# poll cadence: s_sleep 4 instead of 1 in the grid-barrier and hand-off poll loops (fewer polls on the release lines)
# speedup vs baseline: 1.0004x; 1.0004x over previous
; __device__ __forceinline__ unsigned xb_ld(unsigned* p)              { return __hip_atomic_load(p, __ATOMIC_RELAXED, __HIP_MEMORY_SCOPE_AGENT); }
; #define XB_SPIN(cond, bar) do { unsigned _sp = 0; while (cond) { __builtin_amdgcn_s_sleep(1); \
;     if ((++_sp & 255u) == 0u) { if (xb_ld(&(bar)[XB_TMO])) break; if (_sp > XB_SPIN_CAP) { atomicAdd(&(bar)[XB_TMO], 1u); break; } } } } while (0)
; __device__ __forceinline__ void xcd_barrier(const XcdBarrier& b) {
;     ...
;       else XB_SPIN(xb_ld(&bar[XB_TOPGEN]) == tg, bar);
.Lgb_w_1:
	global_load_dword v254, v253, s[44:45] offset:64 sc1
	s_waitcnt vmcnt(0)
	v_cmp_le_u32_e32 vcc, s99, v254
	s_cbranch_vccnz .Lgb_wd_1
	s_sleep 4
	s_add_u32 s100, s100, 1
	s_cmp_lt_u32 s100, 0x1000
	s_cbranch_scc1 .Lgb_w_1

; __device__ __forceinline__ unsigned xb_ld(unsigned* p)              { return __hip_atomic_load(p, __ATOMIC_RELAXED, __HIP_MEMORY_SCOPE_AGENT); }
; #define XB_SPIN(cond, bar) do { unsigned _sp = 0; while (cond) { __builtin_amdgcn_s_sleep(1); \
;     if ((++_sp & 255u) == 0u) { if (xb_ld(&(bar)[XB_TMO])) break; if (_sp > XB_SPIN_CAP) { atomicAdd(&(bar)[XB_TMO], 1u); break; } } } } while (0)
; __device__ __forceinline__ void xcd_barrier(const XcdBarrier& b) {
;     ...
;       XB_SPIN(xb_ld(&bar[XB_XGEN(b.x)]) == gen, bar);
.Lmy_gs_w_8:
	global_load_dword v254, v253, s[44:45] offset:128 sc1
	s_waitcnt vmcnt(0)
	v_cmp_le_u32_e32 vcc, 8, v254
	s_cbranch_vccnz .Lgb_wd_8
	s_sleep 4
	s_add_u32 s100, s100, 1
	s_cmp_lt_u32 s100, 0x100000
	s_cbranch_scc1 .Lmy_gs_w_8
	s_branch .Lgb_wd_8

; __device__ __forceinline__ unsigned xb_ld(unsigned* p)              { return __hip_atomic_load(p, __ATOMIC_RELAXED, __HIP_MEMORY_SCOPE_AGENT); }
; #define XB_SPIN(cond, bar) do { unsigned _sp = 0; while (cond) { __builtin_amdgcn_s_sleep(1); \
;     if ((++_sp & 255u) == 0u) { if (xb_ld(&(bar)[XB_TMO])) break; if (_sp > XB_SPIN_CAP) { atomicAdd(&(bar)[XB_TMO], 1u); break; } } } } while (0)
; __device__ __forceinline__ void xcd_barrier(const XcdBarrier& b) {
;     ...
;       XB_SPIN(xb_ld(&bar[XB_XGEN(b.x)]) == gen, bar);
.Lmy_gs_w_9:
	global_load_dword v254, v253, s[44:45] offset:128 sc1
	s_waitcnt vmcnt(0)
	v_cmp_le_u32_e32 vcc, 16, v254
	s_cbranch_vccnz .Lgb_wd_9
	s_sleep 4
	s_add_u32 s100, s100, 1
	s_cmp_lt_u32 s100, 0x100000
	s_cbranch_scc1 .Lmy_gs_w_9
	s_branch .Lgb_wd_9
